# relation bias folded into the messages: GEMM_A starts the accumulators from rel_b before quantising (as reference h_all = xW + b); agg tail drops the 8 KB/node rel_b loads and count-weighted bias sum
# speedup vs baseline: 1.0114x; 1.0114x over previous
.LBB1_26:
	s_or_b64 exec, exec, s[22:23]
	s_load_dwordx2 s[8:9], s[0:1], 0x40
	s_load_dwordx2 s[10:11], s[0:1], 0x8
	s_load_dwordx4 s[4:7], s[0:1], 0x30
	v_lshlrev_b64 v[44:45], 2, v[8:9]
	v_lshlrev_b32_e32 v42, 10, v1
	v_mov_b32_e32 v43, 0
	s_waitcnt lgkmcnt(0)
	v_max_i32_e32 v25, 1, v25
	v_cvt_f32_u32_e32 v25, v25
	v_div_scale_f32 v46, s[4:5], v25, v25, 1.0
	v_rcp_f32_e32 v52, v46
	v_div_scale_f32 v42, vcc, 1.0, v25, 1.0
	v_fma_f32 v53, -v46, v52, 1.0
	v_fmac_f32_e32 v52, v53, v52
	v_mul_f32_e32 v53, v42, v52
	v_fma_f32 v55, -v46, v53, v42
	v_fmac_f32_e32 v53, v55, v52
	v_fma_f32 v42, -v46, v53, v42
	v_div_fmas_f32 v42, v42, v52, v53
	v_div_fixup_f32 v42, v42, v25, 1.0
	s_waitcnt vmcnt(0)
	v_cvt_f32_f16_e32 v54, v60
	v_cvt_f32_f16_sdwa v55, v60 dst_sel:DWORD dst_unused:UNUSED_PAD src0_sel:WORD_1
	v_cvt_f32_f16_e32 v56, v61
	v_cvt_f32_f16_sdwa v57, v61 dst_sel:DWORD dst_unused:UNUSED_PAD src0_sel:WORD_1
	v_cvt_f32_f16_e32 v58, v62
	v_cvt_f32_f16_sdwa v59, v62 dst_sel:DWORD dst_unused:UNUSED_PAD src0_sel:WORD_1
	v_cvt_f32_f16_e32 v60, v63
	v_cvt_f32_f16_sdwa v61, v63 dst_sel:DWORD dst_unused:UNUSED_PAD src0_sel:WORD_1
	v_lshl_add_u64 v[22:23], s[6:7], 0, v[44:45]
	v_lshl_add_u64 v[44:45], s[8:9], 0, v[44:45]
	v_pk_fma_f32 v[40:41], v[16:17], v[42:43], v[54:55] op_sel_hi:[1,0,1]
	global_load_dwordx4 v[18:21], v[22:23], off
	global_load_dwordx4 v[34:37], v[22:23], off offset:16
	v_pk_fma_f32 v[54:55], v[14:15], v[42:43], v[56:57] op_sel_hi:[1,0,1]
	global_load_dwordx4 v[14:17], v[44:45], off
	v_mov_b32_e32 v22, v40
	v_mov_b32_e32 v23, v41
	global_load_dwordx4 v[38:41], v[44:45], off offset:16
	v_mov_b32_e32 v44, v54
	v_mov_b32_e32 v45, v55
	v_pk_fma_f32 v[12:13], v[12:13], v[42:43], v[58:59] op_sel_hi:[1,0,1]
	v_mov_b32_e32 v25, 0x3b000000
	v_add_f32_e32 v6, 0, v22
	v_add_f32_e32 v6, v6, v23
	v_add_f32_e32 v6, v6, v44
	v_add_f32_e32 v6, v6, v45
	v_mov_b32_e32 v2, v12
	v_mov_b32_e32 v3, v13
	s_nop 0
	v_add_f32_e32 v6, v6, v2
	v_add_f32_e32 v12, v6, v3
	v_pk_fma_f32 v[6:7], v[10:11], v[42:43], v[60:61] op_sel_hi:[1,0,1]
	v_mov_b32_e32 v4, v6
	v_mov_b32_e32 v5, v7
	v_mov_b32_e32 v7, v43
	v_add_f32_e32 v6, v12, v4
	v_add_f32_e32 v6, v6, v5
	s_nop 1
	v_add_f32_dpp v6, v6, v6 quad_perm:[1,0,3,2] row_mask:0xf bank_mask:0xf bound_ctrl:1
	s_nop 1
	v_add_f32_dpp v6, v6, v6 quad_perm:[2,3,0,1] row_mask:0xf bank_mask:0xf bound_ctrl:1
	s_nop 1
	v_add_f32_dpp v6, v6, v6 row_half_mirror row_mask:0xf bank_mask:0xf bound_ctrl:1
	s_nop 1
	v_add_f32_dpp v6, v6, v6 row_mirror row_mask:0xf bank_mask:0xf bound_ctrl:1
	s_nop 1
	v_mov_b32_dpp v7, v6 row_bcast:15 row_mask:0xa bank_mask:0xf
	v_add_f32_e32 v6, v6, v7
	v_mov_b32_e32 v7, v43
	s_nop 1
	v_mov_b32_dpp v7, v6 row_bcast:31 row_mask:0xc bank_mask:0xf
	v_add_f32_e32 v6, v6, v7
	s_nop 0
	v_readlane_b32 s3, v6, 63
	s_nop 1
	v_mul_f32_e32 v6, s3, v25
	v_pk_add_f32 v[8:9], v[22:23], v[6:7] op_sel_hi:[1,0] neg_lo:[0,1] neg_hi:[0,1]
	v_pk_add_f32 v[12:13], v[44:45], v[6:7] op_sel_hi:[1,0] neg_lo:[0,1] neg_hi:[0,1]
	v_pk_mul_f32 v[10:11], v[8:9], v[8:9]
	v_pk_mul_f32 v[22:23], v[12:13], v[12:13]
	v_add_f32_e32 v10, v10, v11
	v_pk_add_f32 v[2:3], v[2:3], v[6:7] op_sel_hi:[1,0] neg_lo:[0,1] neg_hi:[0,1]
	v_add_f32_e32 v10, v10, v22
	v_pk_mul_f32 v[26:27], v[2:3], v[2:3]
	v_add_f32_e32 v10, v10, v23
	v_pk_add_f32 v[4:5], v[4:5], v[6:7] op_sel_hi:[1,0] neg_lo:[0,1] neg_hi:[0,1]
	v_add_f32_e32 v10, v10, v26
	v_pk_mul_f32 v[6:7], v[4:5], v[4:5]
	v_add_f32_e32 v10, v10, v27
	v_add_f32_e32 v6, v10, v6
	v_add_f32_e32 v6, v6, v7
	v_mov_b32_e32 v7, v43
	s_nop 0
	v_add_f32_dpp v6, v6, v6 quad_perm:[1,0,3,2] row_mask:0xf bank_mask:0xf bound_ctrl:1
	s_nop 1
	v_add_f32_dpp v6, v6, v6 quad_perm:[2,3,0,1] row_mask:0xf bank_mask:0xf bound_ctrl:1
	s_nop 1
	v_add_f32_dpp v6, v6, v6 row_half_mirror row_mask:0xf bank_mask:0xf bound_ctrl:1
	s_nop 1
	v_add_f32_dpp v6, v6, v6 row_mirror row_mask:0xf bank_mask:0xf bound_ctrl:1
	s_nop 1
	v_mov_b32_dpp v7, v6 row_bcast:15 row_mask:0xa bank_mask:0xf
	v_add_f32_e32 v6, v6, v7
	s_nop 1
	v_mov_b32_dpp v43, v6 row_bcast:31 row_mask:0xc bank_mask:0xf
	v_add_f32_e32 v6, v6, v43
	s_nop 0
	v_readlane_b32 s3, v6, 63
	v_mov_b32_e32 v6, 0x3727c5ac
	s_nop 0
	v_fmac_f32_e32 v6, s3, v25
	s_mov_b32 s3, 0x800000
	v_mul_f32_e32 v7, 0x4b800000, v6
	v_cmp_gt_f32_e32 vcc, s3, v6
	s_movk_i32 s3, 0x2800
	s_nop 0
	v_cndmask_b32_e32 v6, v6, v7, vcc
	v_rsq_f32_e32 v6, v6
	v_lshrrev_b32_e32 v7, 3, v24
	v_mad_u32_u24 v1, v7, s3, v1
	v_mul_f32_e32 v7, 0x45800000, v6
	v_cndmask_b32_e32 v6, v6, v7, vcc
	v_pk_mul_f32 v[2:3], v[2:3], v[6:7] op_sel_hi:[1,0]
	v_pk_mul_f32 v[10:11], v[12:13], v[6:7] op_sel_hi:[1,0]
	s_waitcnt vmcnt(0)
	v_pk_fma_f32 v[12:13], v[34:35], v[2:3], v[38:39]
	v_pk_mul_f32 v[2:3], v[4:5], v[6:7] op_sel_hi:[1,0]
	v_pk_mul_f32 v[8:9], v[8:9], v[6:7] op_sel_hi:[1,0]
	v_pk_fma_f32 v[6:7], v[36:37], v[2:3], v[40:41]
	v_pk_fma_f32 v[8:9], v[18:19], v[8:9], v[14:15]
	v_cvt_pk_f16_f32 v5, v6, v7
	v_lshlrev_b32_e32 v6, 4, v0
	v_pk_fma_f32 v[10:11], v[20:21], v[10:11], v[16:17]
	v_and_b32_e32 v6, 0x70, v6
	v_cvt_pk_f16_f32 v2, v8, v9
	v_cvt_pk_f16_f32 v3, v10, v11
	v_cvt_pk_f16_f32 v4, v12, v13
	v_lshl_or_b32 v1, v1, 7, v6
	global_store_dwordx4 v1, v[2:5], s[20:21]

LgA_map_done:
	s_load_dwordx4 s[4:7], s[0:1], 0x0
	s_load_dwordx4 s[8:11], s[0:1], 0x20
	s_load_dwordx4 s[12:15], s[0:1], 0x30
	s_load_dwordx2 s[16:17], s[0:1], 0x40
	v_lshrrev_b32_e32 v20, 6, v0
	v_and_b32_e32 v1, 63, v0
	v_readfirstlane_b32 s20, v20
	v_and_b32_e32 v2, 15, v0
	v_bfe_u32 v3, v0, 4, 2
	v_and_b32_e32 v16, 7, v2
	v_xor_b32_e32 v16, v16, v3
	v_lshlrev_b32_e32 v16, 4, v16
	v_lshl_or_b32 v4, v2, 7, v16
	v_lshrrev_b32_e32 v16, 3, v1
	v_and_b32_e32 v17, 7, v1
	v_xor_b32_e32 v17, v17, v16
	v_lshlrev_b32_e32 v17, 4, v17
	v_lshl_or_b32 v9, v16, 7, v17
	v_add_u32_e32 v10, 0x140000, v9
	s_waitcnt lgkmcnt(0)
	s_mul_i32 s36, s20, 0x280000
	s_lshl_b32 s37, s23, 11
	s_add_u32 s36, s36, s37
	s_add_u32 s26, s4, s36
	s_addc_u32 s27, s5, 0
	s_mul_i32 s28, s20, 0x1000
	s_add_u32 s46, s28, 0x14000
	s_mov_b32 s47, s28
	s_mov_b32 s29, 0
	s_cmp_ge_u32 s21, 8
	s_cbranch_scc1 LgA_setup_self
	s_lshl_b32 s36, s21, 8
	s_lshl_b32 s37, s20, 6
	s_add_u32 s36, s36, s37
	v_lshlrev_b32_e32 v16, 4, v3
	v_add_u32_e32 v16, s36, v16
	v_lshlrev_b32_e32 v17, 2, v16
	global_load_dwordx4 v[32:35], v17, s[8:9] offset:0
	global_load_dwordx4 v[36:39], v17, s[8:9] offset:16
	global_load_dwordx4 v[40:43], v17, s[8:9] offset:32
	global_load_dwordx4 v[44:47], v17, s[8:9] offset:48
	v_mul_u32_u24_e32 v16, 2176, v2
	v_lshl_add_u32 v14, v3, 4, v16
	s_lshr_b32 s36, s21, 1
	s_lshl_b32 s37, s23, 6
	s_add_u32 s36, s36, s37
	s_mul_i32 s36, s36, 544
	s_and_b32 s37, s21, 1
	s_lshl_b32 s38, s37, 8
	s_lshl_b32 s39, s20, 6
	s_add_u32 s38, s38, s39
	s_add_u32 s36, s36, s38
	s_add_u32 s30, s12, s36
	s_addc_u32 s31, s13, 0
	s_mul_i32 s37, s37, 240
	s_mul_i32 s39, s20, 60
	s_add_u32 s37, s37, s39
	s_sub_u32 s37, 512, s37
	v_add_u32_e32 v112, s37, v16
	s_mov_b32 s44, 0x0c0c0400
	s_mov_b32 s45, 0x05040100
	s_branch LgA_setup_done

LgA_setup_done:
	s_mov_b32 m0, s28
	s_add_u32 s28, s28, 0x4000
	s_cmp_ge_u32 s28, s46
	s_cselect_b32 s28, s47, s28
	global_load_lds_dwordx4 v9, s[26:27]
	global_load_lds_dwordx4 v9, s[26:27] offset:1024
	s_add_u32 m0, m0, 0x800
	s_nop 0
	global_load_lds_dwordx4 v10, s[26:27]
	global_load_lds_dwordx4 v10, s[26:27] offset:1024
	s_add_u32 s26, s26, 0x800
	s_addc_u32 s27, s27, 0
	s_mov_b32 m0, s28
	s_add_u32 s28, s28, 0x4000
	s_cmp_ge_u32 s28, s46
	s_cselect_b32 s28, s47, s28
	global_load_lds_dwordx4 v9, s[26:27]
	global_load_lds_dwordx4 v9, s[26:27] offset:1024
	s_add_u32 m0, m0, 0x800
	s_nop 0
	global_load_lds_dwordx4 v10, s[26:27]
	global_load_lds_dwordx4 v10, s[26:27] offset:1024
	s_add_u32 s26, s26, 0x800
	s_addc_u32 s27, s27, 0
	s_lshl_b32 s36, s21, 2
	s_add_u32 s36, s36, s20
	s_mul_i32 s36, s36, 0x10000
	v_lshlrev_b32_e32 v16, 4, v1
	v_add_u32_e32 v13, s36, v16
	global_load_dwordx4 a[0:3], v13, s[6:7] offset:0
	global_load_dwordx4 a[4:7], v13, s[6:7] offset:1024
	global_load_dwordx4 a[8:11], v13, s[6:7] offset:2048
	global_load_dwordx4 a[12:15], v13, s[6:7] offset:3072
	v_add_u32_e32 v13, 0x1000, v13
	global_load_dwordx4 a[16:19], v13, s[6:7] offset:0
	global_load_dwordx4 a[20:23], v13, s[6:7] offset:1024
	global_load_dwordx4 a[24:27], v13, s[6:7] offset:2048
	global_load_dwordx4 a[28:31], v13, s[6:7] offset:3072
	v_add_u32_e32 v13, 0x1000, v13
	global_load_dwordx4 a[32:35], v13, s[6:7] offset:0
	global_load_dwordx4 a[36:39], v13, s[6:7] offset:1024
	global_load_dwordx4 a[40:43], v13, s[6:7] offset:2048
	global_load_dwordx4 a[44:47], v13, s[6:7] offset:3072
	v_add_u32_e32 v13, 0x1000, v13
	global_load_dwordx4 a[48:51], v13, s[6:7] offset:0
	global_load_dwordx4 a[52:55], v13, s[6:7] offset:1024
	global_load_dwordx4 a[56:59], v13, s[6:7] offset:2048
	global_load_dwordx4 a[60:63], v13, s[6:7] offset:3072
	v_add_u32_e32 v13, 0x1000, v13
	global_load_dwordx4 a[64:67], v13, s[6:7] offset:0
	global_load_dwordx4 a[68:71], v13, s[6:7] offset:1024
	global_load_dwordx4 a[72:75], v13, s[6:7] offset:2048
	global_load_dwordx4 a[76:79], v13, s[6:7] offset:3072
	v_add_u32_e32 v13, 0x1000, v13
	global_load_dwordx4 a[80:83], v13, s[6:7] offset:0
	global_load_dwordx4 a[84:87], v13, s[6:7] offset:1024
	global_load_dwordx4 a[88:91], v13, s[6:7] offset:2048
	global_load_dwordx4 a[92:95], v13, s[6:7] offset:3072
	v_add_u32_e32 v13, 0x1000, v13
	global_load_dwordx4 a[96:99], v13, s[6:7] offset:0
	global_load_dwordx4 a[100:103], v13, s[6:7] offset:1024
	global_load_dwordx4 a[104:107], v13, s[6:7] offset:2048
	global_load_dwordx4 a[108:111], v13, s[6:7] offset:3072
	v_add_u32_e32 v13, 0x1000, v13
	global_load_dwordx4 a[112:115], v13, s[6:7] offset:0
	global_load_dwordx4 a[116:119], v13, s[6:7] offset:1024
	global_load_dwordx4 a[120:123], v13, s[6:7] offset:2048
	global_load_dwordx4 a[124:127], v13, s[6:7] offset:3072
	v_add_u32_e32 v13, 0x1000, v13
	global_load_dwordx4 a[128:131], v13, s[6:7] offset:0
	global_load_dwordx4 a[132:135], v13, s[6:7] offset:1024
	global_load_dwordx4 a[136:139], v13, s[6:7] offset:2048
	global_load_dwordx4 a[140:143], v13, s[6:7] offset:3072
	v_add_u32_e32 v13, 0x1000, v13
	global_load_dwordx4 a[144:147], v13, s[6:7] offset:0
	global_load_dwordx4 a[148:151], v13, s[6:7] offset:1024
	global_load_dwordx4 a[152:155], v13, s[6:7] offset:2048
	global_load_dwordx4 a[156:159], v13, s[6:7] offset:3072
	v_add_u32_e32 v13, 0x1000, v13
	global_load_dwordx4 a[160:163], v13, s[6:7] offset:0
	global_load_dwordx4 a[164:167], v13, s[6:7] offset:1024
	global_load_dwordx4 a[168:171], v13, s[6:7] offset:2048
	global_load_dwordx4 a[172:175], v13, s[6:7] offset:3072
	v_add_u32_e32 v13, 0x1000, v13
	global_load_dwordx4 a[176:179], v13, s[6:7] offset:0
	global_load_dwordx4 a[180:183], v13, s[6:7] offset:1024
	global_load_dwordx4 a[184:187], v13, s[6:7] offset:2048
	global_load_dwordx4 a[188:191], v13, s[6:7] offset:3072
	v_add_u32_e32 v13, 0x1000, v13
	global_load_dwordx4 a[192:195], v13, s[6:7] offset:0
	global_load_dwordx4 a[196:199], v13, s[6:7] offset:1024
	global_load_dwordx4 a[200:203], v13, s[6:7] offset:2048
	global_load_dwordx4 a[204:207], v13, s[6:7] offset:3072
	v_add_u32_e32 v13, 0x1000, v13
	global_load_dwordx4 a[208:211], v13, s[6:7] offset:0
	global_load_dwordx4 a[212:215], v13, s[6:7] offset:1024
	global_load_dwordx4 a[216:219], v13, s[6:7] offset:2048
	global_load_dwordx4 a[220:223], v13, s[6:7] offset:3072
	v_add_u32_e32 v13, 0x1000, v13
	global_load_dwordx4 a[224:227], v13, s[6:7] offset:0
	global_load_dwordx4 a[228:231], v13, s[6:7] offset:1024
	global_load_dwordx4 a[232:235], v13, s[6:7] offset:2048
	global_load_dwordx4 a[236:239], v13, s[6:7] offset:3072
	v_add_u32_e32 v13, 0x1000, v13
	global_load_dwordx4 a[240:243], v13, s[6:7] offset:0
	global_load_dwordx4 a[244:247], v13, s[6:7] offset:1024
	global_load_dwordx4 a[248:251], v13, s[6:7] offset:2048
	global_load_dwordx4 a[252:255], v13, s[6:7] offset:3072
	s_mov_b32 m0, s28
	s_add_u32 s28, s28, 0x4000
	s_cmp_ge_u32 s28, s46
	s_cselect_b32 s28, s47, s28
	global_load_lds_dwordx4 v9, s[26:27]
	global_load_lds_dwordx4 v9, s[26:27] offset:1024
	s_add_u32 m0, m0, 0x800
	s_nop 0
	global_load_lds_dwordx4 v10, s[26:27]
	global_load_lds_dwordx4 v10, s[26:27] offset:1024
	s_add_u32 s26, s26, 0x800
	s_addc_u32 s27, s27, 0
	s_mov_b32 m0, s28
	s_add_u32 s28, s28, 0x4000
	s_cmp_ge_u32 s28, s46
	s_cselect_b32 s28, s47, s28
	global_load_lds_dwordx4 v9, s[26:27]
	global_load_lds_dwordx4 v9, s[26:27] offset:1024
	s_add_u32 m0, m0, 0x800
	s_nop 0
	global_load_lds_dwordx4 v10, s[26:27]
	global_load_lds_dwordx4 v10, s[26:27] offset:1024
	s_add_u32 s26, s26, 0x800
	s_addc_u32 s27, s27, 0
	s_waitcnt vmcnt(63)
	s_barrier
	v_add_u32_e32 v5, s29, v4
	v_xor_b32_e32 v6, 64, v5
	s_add_u32 s29, s29, 0x4000
	s_cmp_ge_u32 s29, 0x14000
	s_cselect_b32 s29, 0, s29
	ds_read_b128 v[128:131], v5 offset:0
	ds_read_b128 v[132:135], v6 offset:0
	ds_read_b128 v[136:139], v5 offset:2048
	ds_read_b128 v[140:143], v6 offset:2048
	ds_read_b128 v[144:147], v5 offset:4096
	ds_read_b128 v[148:151], v6 offset:4096
	ds_read_b128 v[152:155], v5 offset:6144
	ds_read_b128 v[156:159], v6 offset:6144
	ds_read_b128 v[160:163], v5 offset:8192
	ds_read_b128 v[164:167], v6 offset:8192
	ds_read_b128 v[168:171], v5 offset:10240
	ds_read_b128 v[172:175], v6 offset:10240
	ds_read_b128 v[176:179], v5 offset:12288
	ds_read_b128 v[180:183], v6 offset:12288
	ds_read_b128 v[184:187], v5 offset:14336
	ds_read_b128 v[188:191], v6 offset:14336
	s_waitcnt lgkmcnt(0)
	s_cmp_ge_u32 s21, 8
	s_cbranch_scc1 LgA_self_body
	s_mov_b32 m0, s28
	s_add_u32 s28, s28, 0x4000
	s_cmp_ge_u32 s28, s46
	s_cselect_b32 s28, s47, s28
	global_load_lds_dwordx4 v9, s[26:27]
	global_load_lds_dwordx4 v9, s[26:27] offset:1024
	s_add_u32 m0, m0, 0x800
	s_nop 0
	global_load_lds_dwordx4 v10, s[26:27]
	global_load_lds_dwordx4 v10, s[26:27] offset:1024
	s_add_u32 s26, s26, 0x800
	s_addc_u32 s27, s27, 0
	v_add_u32_e32 v7, s29, v4
	v_xor_b32_e32 v8, 64, v7
	s_add_u32 s29, s29, 0x4000
	s_cmp_ge_u32 s29, 0x14000
	s_cselect_b32 s29, 0, s29
	s_waitcnt vmcnt(63)
	v_mfma_f32_16x16x32_f16 v[48:51], a[0:3], v[128:131], v[32:35]
	v_mfma_f32_16x16x32_f16 v[52:55], a[4:7], v[128:131], v[36:39]
	v_mfma_f32_16x16x32_f16 v[56:59], a[8:11], v[128:131], v[40:43]
	ds_read_b128 v[192:195], v7 offset:0
	v_mfma_f32_16x16x32_f16 v[60:63], a[12:15], v[128:131], v[44:47]
	ds_read_b128 v[196:199], v8 offset:0
	s_waitcnt vmcnt(63)
	v_mfma_f32_16x16x32_f16 v[48:51], a[16:19], v[132:135], v[48:51]
	ds_read_b128 v[200:203], v7 offset:2048
	v_mfma_f32_16x16x32_f16 v[52:55], a[20:23], v[132:135], v[52:55]
	ds_read_b128 v[204:207], v8 offset:2048
	v_mfma_f32_16x16x32_f16 v[56:59], a[24:27], v[132:135], v[56:59]
	ds_read_b128 v[208:211], v7 offset:4096
	v_mfma_f32_16x16x32_f16 v[60:63], a[28:31], v[132:135], v[60:63]
	ds_read_b128 v[212:215], v8 offset:4096
	s_waitcnt vmcnt(63)
	v_mfma_f32_16x16x32_f16 v[48:51], a[32:35], v[136:139], v[48:51]
	ds_read_b128 v[216:219], v7 offset:6144
	v_mfma_f32_16x16x32_f16 v[52:55], a[36:39], v[136:139], v[52:55]
	ds_read_b128 v[220:223], v8 offset:6144
	v_mfma_f32_16x16x32_f16 v[56:59], a[40:43], v[136:139], v[56:59]
	ds_read_b128 v[224:227], v7 offset:8192
	v_mfma_f32_16x16x32_f16 v[60:63], a[44:47], v[136:139], v[60:63]
	ds_read_b128 v[228:231], v8 offset:8192
	s_waitcnt vmcnt(60)
	v_mfma_f32_16x16x32_f16 v[48:51], a[48:51], v[140:143], v[48:51]
	ds_read_b128 v[232:235], v7 offset:10240
	v_mfma_f32_16x16x32_f16 v[52:55], a[52:55], v[140:143], v[52:55]
	ds_read_b128 v[236:239], v8 offset:10240
	v_mfma_f32_16x16x32_f16 v[56:59], a[56:59], v[140:143], v[56:59]
	ds_read_b128 v[240:243], v7 offset:12288
	v_mfma_f32_16x16x32_f16 v[60:63], a[60:63], v[140:143], v[60:63]
	ds_read_b128 v[244:247], v8 offset:12288
	s_waitcnt vmcnt(56)
	v_mfma_f32_16x16x32_f16 v[48:51], a[64:67], v[144:147], v[48:51]
	ds_read_b128 v[248:251], v7 offset:14336
	v_mfma_f32_16x16x32_f16 v[52:55], a[68:71], v[144:147], v[52:55]
	ds_read_b128 v[252:255], v8 offset:14336
	v_mfma_f32_16x16x32_f16 v[56:59], a[72:75], v[144:147], v[56:59]
	v_mfma_f32_16x16x32_f16 v[60:63], a[76:79], v[144:147], v[60:63]
	s_waitcnt vmcnt(52)
	v_mfma_f32_16x16x32_f16 v[48:51], a[80:83], v[148:151], v[48:51]
	v_mfma_f32_16x16x32_f16 v[52:55], a[84:87], v[148:151], v[52:55]
	v_mfma_f32_16x16x32_f16 v[56:59], a[88:91], v[148:151], v[56:59]
	v_mfma_f32_16x16x32_f16 v[60:63], a[92:95], v[148:151], v[60:63]
	s_waitcnt vmcnt(48)
	v_mfma_f32_16x16x32_f16 v[48:51], a[96:99], v[152:155], v[48:51]
	v_mfma_f32_16x16x32_f16 v[52:55], a[100:103], v[152:155], v[52:55]
	v_mfma_f32_16x16x32_f16 v[56:59], a[104:107], v[152:155], v[56:59]
	v_mfma_f32_16x16x32_f16 v[60:63], a[108:111], v[152:155], v[60:63]
	s_waitcnt vmcnt(44)
	v_mfma_f32_16x16x32_f16 v[48:51], a[112:115], v[156:159], v[48:51]
	v_mfma_f32_16x16x32_f16 v[52:55], a[116:119], v[156:159], v[52:55]
	v_mfma_f32_16x16x32_f16 v[56:59], a[120:123], v[156:159], v[56:59]
	v_mfma_f32_16x16x32_f16 v[60:63], a[124:127], v[156:159], v[60:63]
	s_waitcnt vmcnt(40)
	v_mfma_f32_16x16x32_f16 v[48:51], a[128:131], v[160:163], v[48:51]
	v_mfma_f32_16x16x32_f16 v[52:55], a[132:135], v[160:163], v[52:55]
	v_mfma_f32_16x16x32_f16 v[56:59], a[136:139], v[160:163], v[56:59]
	v_mfma_f32_16x16x32_f16 v[60:63], a[140:143], v[160:163], v[60:63]
	s_waitcnt vmcnt(36)
	v_mfma_f32_16x16x32_f16 v[48:51], a[144:147], v[164:167], v[48:51]
	v_mfma_f32_16x16x32_f16 v[52:55], a[148:151], v[164:167], v[52:55]
	v_mfma_f32_16x16x32_f16 v[56:59], a[152:155], v[164:167], v[56:59]
	v_mfma_f32_16x16x32_f16 v[60:63], a[156:159], v[164:167], v[60:63]
	s_waitcnt vmcnt(32)
	v_mfma_f32_16x16x32_f16 v[48:51], a[160:163], v[168:171], v[48:51]
	v_mfma_f32_16x16x32_f16 v[52:55], a[164:167], v[168:171], v[52:55]
	v_mfma_f32_16x16x32_f16 v[56:59], a[168:171], v[168:171], v[56:59]
	v_mfma_f32_16x16x32_f16 v[60:63], a[172:175], v[168:171], v[60:63]
	s_waitcnt vmcnt(28)
	v_mfma_f32_16x16x32_f16 v[48:51], a[176:179], v[172:175], v[48:51]
	v_mfma_f32_16x16x32_f16 v[52:55], a[180:183], v[172:175], v[52:55]
	v_mfma_f32_16x16x32_f16 v[56:59], a[184:187], v[172:175], v[56:59]
	v_mfma_f32_16x16x32_f16 v[60:63], a[188:191], v[172:175], v[60:63]
	s_waitcnt vmcnt(24)
	v_mfma_f32_16x16x32_f16 v[48:51], a[192:195], v[176:179], v[48:51]
	v_mfma_f32_16x16x32_f16 v[52:55], a[196:199], v[176:179], v[52:55]
	v_mfma_f32_16x16x32_f16 v[56:59], a[200:203], v[176:179], v[56:59]
	v_mfma_f32_16x16x32_f16 v[60:63], a[204:207], v[176:179], v[60:63]
	s_waitcnt vmcnt(20)
	v_mfma_f32_16x16x32_f16 v[48:51], a[208:211], v[180:183], v[48:51]
	v_mfma_f32_16x16x32_f16 v[52:55], a[212:215], v[180:183], v[52:55]
	v_mfma_f32_16x16x32_f16 v[56:59], a[216:219], v[180:183], v[56:59]
	v_mfma_f32_16x16x32_f16 v[60:63], a[220:223], v[180:183], v[60:63]
	s_waitcnt vmcnt(16)
	v_mfma_f32_16x16x32_f16 v[48:51], a[224:227], v[184:187], v[48:51]
	v_mfma_f32_16x16x32_f16 v[52:55], a[228:231], v[184:187], v[52:55]
	v_mfma_f32_16x16x32_f16 v[56:59], a[232:235], v[184:187], v[56:59]
	v_mfma_f32_16x16x32_f16 v[60:63], a[236:239], v[184:187], v[60:63]
	s_waitcnt vmcnt(12)
	v_mfma_f32_16x16x32_f16 v[48:51], a[240:243], v[188:191], v[48:51]
	v_mfma_f32_16x16x32_f16 v[52:55], a[244:247], v[188:191], v[52:55]
	v_mfma_f32_16x16x32_f16 v[56:59], a[248:251], v[188:191], v[56:59]
	v_mfma_f32_16x16x32_f16 v[60:63], a[252:255], v[188:191], v[60:63]
LgAq_loop:
	s_waitcnt vmcnt(8) lgkmcnt(0)
	s_barrier
	v_mfma_f32_16x16x32_f16 v[64:67], a[0:3], v[192:195], v[32:35]
	v_mfma_f32_16x16x32_f16 v[68:71], a[4:7], v[192:195], v[36:39]
	v_add_u32_e32 v5, s29, v4
	v_xor_b32_e32 v6, 64, v5
	s_add_u32 s29, s29, 0x4000
	s_cmp_ge_u32 s29, 0x14000
	s_cselect_b32 s29, 0, s29
	v_mfma_f32_16x16x32_f16 v[72:75], a[8:11], v[192:195], v[40:43]
	ds_read_b128 v[128:131], v5 offset:0
	v_mfma_f32_16x16x32_f16 v[76:79], a[12:15], v[192:195], v[44:47]
	ds_read_b128 v[132:135], v6 offset:0
	v_max3_f32 v16, |v48|, 0, |v49|
	v_mfma_f32_16x16x32_f16 v[64:67], a[16:19], v[196:199], v[64:67]
	ds_read_b128 v[136:139], v5 offset:2048
	v_max3_f32 v16, v16, |v50|, |v51|
	v_mfma_f32_16x16x32_f16 v[68:71], a[20:23], v[196:199], v[68:71]
	ds_read_b128 v[140:143], v6 offset:2048
	v_max3_f32 v16, v16, |v52|, |v53|
	v_mfma_f32_16x16x32_f16 v[72:75], a[24:27], v[196:199], v[72:75]
	ds_read_b128 v[144:147], v5 offset:4096
	v_max3_f32 v16, v16, |v54|, |v55|
	v_mfma_f32_16x16x32_f16 v[76:79], a[28:31], v[196:199], v[76:79]
	ds_read_b128 v[148:151], v6 offset:4096
	v_max3_f32 v16, v16, |v56|, |v57|
	v_mfma_f32_16x16x32_f16 v[64:67], a[32:35], v[200:203], v[64:67]
	ds_read_b128 v[152:155], v5 offset:6144
	v_max3_f32 v16, v16, |v58|, |v59|
	v_mfma_f32_16x16x32_f16 v[68:71], a[36:39], v[200:203], v[68:71]
	ds_read_b128 v[156:159], v6 offset:6144
	v_max3_f32 v16, v16, |v60|, |v61|
	v_mfma_f32_16x16x32_f16 v[72:75], a[40:43], v[200:203], v[72:75]
	ds_read_b128 v[160:163], v5 offset:8192
	v_max3_f32 v16, v16, |v62|, |v63|
	v_mfma_f32_16x16x32_f16 v[76:79], a[44:47], v[200:203], v[76:79]
	ds_read_b128 v[164:167], v6 offset:8192
	v_mov_b32_e32 v17, v16
	v_mfma_f32_16x16x32_f16 v[64:67], a[48:51], v[204:207], v[64:67]
	ds_read_b128 v[168:171], v5 offset:10240
	v_mov_b32_e32 v18, v16
	v_mfma_f32_16x16x32_f16 v[68:71], a[52:55], v[204:207], v[68:71]
	ds_read_b128 v[172:175], v6 offset:10240
	v_permlane32_swap_b32_e32 v17, v18
	v_mfma_f32_16x16x32_f16 v[72:75], a[56:59], v[204:207], v[72:75]
	ds_read_b128 v[176:179], v5 offset:12288
	v_max_f32_e32 v16, v17, v18
	v_mfma_f32_16x16x32_f16 v[76:79], a[60:63], v[204:207], v[76:79]
	ds_read_b128 v[180:183], v6 offset:12288
	v_mov_b32_e32 v17, v16
	v_mfma_f32_16x16x32_f16 v[64:67], a[64:67], v[208:211], v[64:67]
	ds_read_b128 v[184:187], v5 offset:14336
	v_mfma_f32_16x16x32_f16 v[68:71], a[68:71], v[208:211], v[68:71]
	ds_read_b128 v[188:191], v6 offset:14336
	v_mov_b32_e32 v18, v16
	v_mfma_f32_16x16x32_f16 v[72:75], a[72:75], v[208:211], v[72:75]
	s_nop 0
	v_permlane16_swap_b32_e32 v17, v18
	v_mfma_f32_16x16x32_f16 v[76:79], a[76:79], v[208:211], v[76:79]
	v_max_f32_e32 v16, v17, v18
	v_mfma_f32_16x16x32_f16 v[64:67], a[80:83], v[212:215], v[64:67]
	v_rcp_f32_e32 v19, v16
	v_mfma_f32_16x16x32_f16 v[68:71], a[84:87], v[212:215], v[68:71]
	v_cmp_lt_f32_e32 vcc, 0, v16
	v_mfma_f32_16x16x32_f16 v[72:75], a[88:91], v[212:215], v[72:75]
	s_mov_b32 m0, s28
	s_add_u32 s28, s28, 0x4000
	s_cmp_ge_u32 s28, s46
	s_cselect_b32 s28, s47, s28
	global_load_lds_dwordx4 v9, s[26:27]
	v_mul_f32_e32 v19, 0x42fe0000, v19
	v_mfma_f32_16x16x32_f16 v[76:79], a[92:95], v[212:215], v[76:79]
	v_mul_f32_e32 v20, 0x3c010204, v16
	v_mfma_f32_16x16x32_f16 v[64:67], a[96:99], v[216:219], v[64:67]
	v_cndmask_b32_e32 v19, 0, v19, vcc
	v_mfma_f32_16x16x32_f16 v[68:71], a[100:103], v[216:219], v[68:71]
	v_cndmask_b32_e32 v20, 1.0, v20, vcc
	v_mfma_f32_16x16x32_f16 v[72:75], a[104:107], v[216:219], v[72:75]
	v_fmaak_f32 v96, v19, v48, 0x4b400000
	v_mfma_f32_16x16x32_f16 v[76:79], a[108:111], v[216:219], v[76:79]
	v_fmaak_f32 v97, v19, v49, 0x4b400000
	v_mfma_f32_16x16x32_f16 v[64:67], a[112:115], v[220:223], v[64:67]
	v_fmaak_f32 v98, v19, v50, 0x4b400000
	v_mfma_f32_16x16x32_f16 v[68:71], a[116:119], v[220:223], v[68:71]
	v_fmaak_f32 v99, v19, v51, 0x4b400000
	v_mfma_f32_16x16x32_f16 v[72:75], a[120:123], v[220:223], v[72:75]
	v_mfma_f32_16x16x32_f16 v[76:79], a[124:127], v[220:223], v[76:79]
	v_fmaak_f32 v100, v19, v52, 0x4b400000
	v_mfma_f32_16x16x32_f16 v[64:67], a[128:131], v[224:227], v[64:67]
	v_fmaak_f32 v101, v19, v53, 0x4b400000
	v_mfma_f32_16x16x32_f16 v[68:71], a[132:135], v[224:227], v[68:71]
	global_load_lds_dwordx4 v9, s[26:27] offset:1024
	v_fmaak_f32 v102, v19, v54, 0x4b400000
	v_mfma_f32_16x16x32_f16 v[72:75], a[136:139], v[224:227], v[72:75]
	v_fmaak_f32 v103, v19, v55, 0x4b400000
	v_mfma_f32_16x16x32_f16 v[76:79], a[140:143], v[224:227], v[76:79]
	v_fmaak_f32 v104, v19, v56, 0x4b400000
	v_mfma_f32_16x16x32_f16 v[64:67], a[144:147], v[228:231], v[64:67]
	v_fmaak_f32 v105, v19, v57, 0x4b400000
	v_mfma_f32_16x16x32_f16 v[68:71], a[148:151], v[228:231], v[68:71]
	v_fmaak_f32 v106, v19, v58, 0x4b400000
	v_mfma_f32_16x16x32_f16 v[72:75], a[152:155], v[228:231], v[72:75]
	v_fmaak_f32 v107, v19, v59, 0x4b400000
	v_mfma_f32_16x16x32_f16 v[76:79], a[156:159], v[228:231], v[76:79]
	v_fmaak_f32 v108, v19, v60, 0x4b400000
	v_mfma_f32_16x16x32_f16 v[64:67], a[160:163], v[232:235], v[64:67]
	v_fmaak_f32 v109, v19, v61, 0x4b400000
	v_mfma_f32_16x16x32_f16 v[68:71], a[164:167], v[232:235], v[68:71]
	v_fmaak_f32 v110, v19, v62, 0x4b400000
	v_mfma_f32_16x16x32_f16 v[72:75], a[168:171], v[232:235], v[72:75]
	v_fmaak_f32 v111, v19, v63, 0x4b400000
	v_mfma_f32_16x16x32_f16 v[76:79], a[172:175], v[232:235], v[76:79]
	v_perm_b32 v21, v97, v96, s44
	v_mfma_f32_16x16x32_f16 v[64:67], a[176:179], v[236:239], v[64:67]
	s_add_u32 m0, m0, 0x800
	s_nop 0
	global_load_lds_dwordx4 v10, s[26:27]
	v_mfma_f32_16x16x32_f16 v[68:71], a[180:183], v[236:239], v[68:71]
	v_perm_b32 v22, v99, v98, s44
	v_mfma_f32_16x16x32_f16 v[72:75], a[184:187], v[236:239], v[72:75]
	v_perm_b32 v23, v101, v100, s44
	v_mfma_f32_16x16x32_f16 v[76:79], a[188:191], v[236:239], v[76:79]
	v_perm_b32 v24, v103, v102, s44
	v_mfma_f32_16x16x32_f16 v[64:67], a[192:195], v[240:243], v[64:67]
	v_perm_b32 v25, v105, v104, s44
	v_mfma_f32_16x16x32_f16 v[68:71], a[196:199], v[240:243], v[68:71]
	v_perm_b32 v26, v107, v106, s44
	v_mfma_f32_16x16x32_f16 v[72:75], a[200:203], v[240:243], v[72:75]
	v_perm_b32 v27, v109, v108, s44
	v_mfma_f32_16x16x32_f16 v[76:79], a[204:207], v[240:243], v[76:79]
	v_perm_b32 v28, v111, v110, s44
	v_mfma_f32_16x16x32_f16 v[64:67], a[208:211], v[244:247], v[64:67]
	v_perm_b32 v96, v22, v21, s45
	v_mfma_f32_16x16x32_f16 v[68:71], a[212:215], v[244:247], v[68:71]
	v_perm_b32 v97, v24, v23, s45
	v_mfma_f32_16x16x32_f16 v[72:75], a[216:219], v[244:247], v[72:75]
	v_perm_b32 v98, v26, v25, s45
	v_mfma_f32_16x16x32_f16 v[76:79], a[220:223], v[244:247], v[76:79]
	v_perm_b32 v99, v28, v27, s45
	v_mfma_f32_16x16x32_f16 v[64:67], a[224:227], v[248:251], v[64:67]
	global_load_lds_dwordx4 v10, s[26:27] offset:1024
	global_store_dwordx4 v14, v[96:99], s[30:31]
	v_mfma_f32_16x16x32_f16 v[68:71], a[228:231], v[248:251], v[68:71]
	s_add_u32 s26, s26, 0x800
	s_addc_u32 s27, s27, 0
	global_store_dword v112, v20, s[30:31]
	v_mfma_f32_16x16x32_f16 v[72:75], a[232:235], v[248:251], v[72:75]
	v_mfma_f32_16x16x32_f16 v[76:79], a[236:239], v[248:251], v[76:79]
	s_add_u32 s30, s30, 0x8800
	s_addc_u32 s31, s31, 0
	v_mfma_f32_16x16x32_f16 v[64:67], a[240:243], v[252:255], v[64:67]
	v_mfma_f32_16x16x32_f16 v[68:71], a[244:247], v[252:255], v[68:71]
	v_mfma_f32_16x16x32_f16 v[72:75], a[248:251], v[252:255], v[72:75]
	v_mfma_f32_16x16x32_f16 v[76:79], a[252:255], v[252:255], v[76:79]
	s_sub_u32 s24, s24, 1
	s_cmp_le_u32 s24, 1
	s_cbranch_scc1 LgAq_exitA
	s_waitcnt vmcnt(8) lgkmcnt(0)
	s_barrier
	v_mfma_f32_16x16x32_f16 v[48:51], a[0:3], v[128:131], v[32:35]
	v_mfma_f32_16x16x32_f16 v[52:55], a[4:7], v[128:131], v[36:39]
	v_add_u32_e32 v7, s29, v4
	v_xor_b32_e32 v8, 64, v7
	s_add_u32 s29, s29, 0x4000
	s_cmp_ge_u32 s29, 0x14000
	s_cselect_b32 s29, 0, s29
	v_mfma_f32_16x16x32_f16 v[56:59], a[8:11], v[128:131], v[40:43]
	ds_read_b128 v[192:195], v7 offset:0
	v_mfma_f32_16x16x32_f16 v[60:63], a[12:15], v[128:131], v[44:47]
	ds_read_b128 v[196:199], v8 offset:0
	v_max3_f32 v16, |v64|, 0, |v65|
	v_mfma_f32_16x16x32_f16 v[48:51], a[16:19], v[132:135], v[48:51]
	ds_read_b128 v[200:203], v7 offset:2048
	v_max3_f32 v16, v16, |v66|, |v67|
	v_mfma_f32_16x16x32_f16 v[52:55], a[20:23], v[132:135], v[52:55]
	ds_read_b128 v[204:207], v8 offset:2048
	v_max3_f32 v16, v16, |v68|, |v69|
	v_mfma_f32_16x16x32_f16 v[56:59], a[24:27], v[132:135], v[56:59]
	ds_read_b128 v[208:211], v7 offset:4096
	v_max3_f32 v16, v16, |v70|, |v71|
	v_mfma_f32_16x16x32_f16 v[60:63], a[28:31], v[132:135], v[60:63]
	ds_read_b128 v[212:215], v8 offset:4096
	v_max3_f32 v16, v16, |v72|, |v73|
	v_mfma_f32_16x16x32_f16 v[48:51], a[32:35], v[136:139], v[48:51]
	ds_read_b128 v[216:219], v7 offset:6144
	v_max3_f32 v16, v16, |v74|, |v75|
	v_mfma_f32_16x16x32_f16 v[52:55], a[36:39], v[136:139], v[52:55]
	ds_read_b128 v[220:223], v8 offset:6144
	v_max3_f32 v16, v16, |v76|, |v77|
	v_mfma_f32_16x16x32_f16 v[56:59], a[40:43], v[136:139], v[56:59]
	ds_read_b128 v[224:227], v7 offset:8192
	v_max3_f32 v16, v16, |v78|, |v79|
	v_mfma_f32_16x16x32_f16 v[60:63], a[44:47], v[136:139], v[60:63]
	ds_read_b128 v[228:231], v8 offset:8192
	v_mov_b32_e32 v17, v16
	v_mfma_f32_16x16x32_f16 v[48:51], a[48:51], v[140:143], v[48:51]
	ds_read_b128 v[232:235], v7 offset:10240
	v_mov_b32_e32 v18, v16
	v_mfma_f32_16x16x32_f16 v[52:55], a[52:55], v[140:143], v[52:55]
	ds_read_b128 v[236:239], v8 offset:10240
	v_permlane32_swap_b32_e32 v17, v18
	v_mfma_f32_16x16x32_f16 v[56:59], a[56:59], v[140:143], v[56:59]
	ds_read_b128 v[240:243], v7 offset:12288
	v_max_f32_e32 v16, v17, v18
	v_mfma_f32_16x16x32_f16 v[60:63], a[60:63], v[140:143], v[60:63]
	ds_read_b128 v[244:247], v8 offset:12288
	v_mov_b32_e32 v17, v16
	v_mfma_f32_16x16x32_f16 v[48:51], a[64:67], v[144:147], v[48:51]
	ds_read_b128 v[248:251], v7 offset:14336
	v_mfma_f32_16x16x32_f16 v[52:55], a[68:71], v[144:147], v[52:55]
	ds_read_b128 v[252:255], v8 offset:14336
	v_mov_b32_e32 v18, v16
	v_mfma_f32_16x16x32_f16 v[56:59], a[72:75], v[144:147], v[56:59]
	s_nop 0
	v_permlane16_swap_b32_e32 v17, v18
	v_mfma_f32_16x16x32_f16 v[60:63], a[76:79], v[144:147], v[60:63]
	v_max_f32_e32 v16, v17, v18
	v_mfma_f32_16x16x32_f16 v[48:51], a[80:83], v[148:151], v[48:51]
	v_rcp_f32_e32 v19, v16
	v_mfma_f32_16x16x32_f16 v[52:55], a[84:87], v[148:151], v[52:55]
	v_cmp_lt_f32_e32 vcc, 0, v16
	v_mfma_f32_16x16x32_f16 v[56:59], a[88:91], v[148:151], v[56:59]
	s_mov_b32 m0, s28
	s_add_u32 s28, s28, 0x4000
	s_cmp_ge_u32 s28, s46
	s_cselect_b32 s28, s47, s28
	global_load_lds_dwordx4 v9, s[26:27]
	v_mul_f32_e32 v19, 0x42fe0000, v19
	v_mfma_f32_16x16x32_f16 v[60:63], a[92:95], v[148:151], v[60:63]
	v_mul_f32_e32 v20, 0x3c010204, v16
	v_mfma_f32_16x16x32_f16 v[48:51], a[96:99], v[152:155], v[48:51]
	v_cndmask_b32_e32 v19, 0, v19, vcc
	v_mfma_f32_16x16x32_f16 v[52:55], a[100:103], v[152:155], v[52:55]
	v_cndmask_b32_e32 v20, 1.0, v20, vcc
	v_mfma_f32_16x16x32_f16 v[56:59], a[104:107], v[152:155], v[56:59]
	v_fmaak_f32 v96, v19, v64, 0x4b400000
	v_mfma_f32_16x16x32_f16 v[60:63], a[108:111], v[152:155], v[60:63]
	v_fmaak_f32 v97, v19, v65, 0x4b400000
	v_mfma_f32_16x16x32_f16 v[48:51], a[112:115], v[156:159], v[48:51]
	v_fmaak_f32 v98, v19, v66, 0x4b400000
	v_mfma_f32_16x16x32_f16 v[52:55], a[116:119], v[156:159], v[52:55]
	v_fmaak_f32 v99, v19, v67, 0x4b400000
	v_mfma_f32_16x16x32_f16 v[56:59], a[120:123], v[156:159], v[56:59]
	v_mfma_f32_16x16x32_f16 v[60:63], a[124:127], v[156:159], v[60:63]
	v_fmaak_f32 v100, v19, v68, 0x4b400000
	v_mfma_f32_16x16x32_f16 v[48:51], a[128:131], v[160:163], v[48:51]
	v_fmaak_f32 v101, v19, v69, 0x4b400000
	v_mfma_f32_16x16x32_f16 v[52:55], a[132:135], v[160:163], v[52:55]
	global_load_lds_dwordx4 v9, s[26:27] offset:1024
	v_fmaak_f32 v102, v19, v70, 0x4b400000
	v_mfma_f32_16x16x32_f16 v[56:59], a[136:139], v[160:163], v[56:59]
	v_fmaak_f32 v103, v19, v71, 0x4b400000
	v_mfma_f32_16x16x32_f16 v[60:63], a[140:143], v[160:163], v[60:63]
	v_fmaak_f32 v104, v19, v72, 0x4b400000
	v_mfma_f32_16x16x32_f16 v[48:51], a[144:147], v[164:167], v[48:51]
	v_fmaak_f32 v105, v19, v73, 0x4b400000
	v_mfma_f32_16x16x32_f16 v[52:55], a[148:151], v[164:167], v[52:55]
	v_fmaak_f32 v106, v19, v74, 0x4b400000
	v_mfma_f32_16x16x32_f16 v[56:59], a[152:155], v[164:167], v[56:59]
	v_fmaak_f32 v107, v19, v75, 0x4b400000
	v_mfma_f32_16x16x32_f16 v[60:63], a[156:159], v[164:167], v[60:63]
	v_fmaak_f32 v108, v19, v76, 0x4b400000
	v_mfma_f32_16x16x32_f16 v[48:51], a[160:163], v[168:171], v[48:51]
	v_fmaak_f32 v109, v19, v77, 0x4b400000
	v_mfma_f32_16x16x32_f16 v[52:55], a[164:167], v[168:171], v[52:55]
	v_fmaak_f32 v110, v19, v78, 0x4b400000
	v_mfma_f32_16x16x32_f16 v[56:59], a[168:171], v[168:171], v[56:59]
	v_fmaak_f32 v111, v19, v79, 0x4b400000
	v_mfma_f32_16x16x32_f16 v[60:63], a[172:175], v[168:171], v[60:63]
	v_perm_b32 v21, v97, v96, s44
	v_mfma_f32_16x16x32_f16 v[48:51], a[176:179], v[172:175], v[48:51]
	s_add_u32 m0, m0, 0x800
	s_nop 0
	global_load_lds_dwordx4 v10, s[26:27]
	v_mfma_f32_16x16x32_f16 v[52:55], a[180:183], v[172:175], v[52:55]
	v_perm_b32 v22, v99, v98, s44
	v_mfma_f32_16x16x32_f16 v[56:59], a[184:187], v[172:175], v[56:59]
	v_perm_b32 v23, v101, v100, s44
	v_mfma_f32_16x16x32_f16 v[60:63], a[188:191], v[172:175], v[60:63]
	v_perm_b32 v24, v103, v102, s44
	v_mfma_f32_16x16x32_f16 v[48:51], a[192:195], v[176:179], v[48:51]
	v_perm_b32 v25, v105, v104, s44
	v_mfma_f32_16x16x32_f16 v[52:55], a[196:199], v[176:179], v[52:55]
	v_perm_b32 v26, v107, v106, s44
	v_mfma_f32_16x16x32_f16 v[56:59], a[200:203], v[176:179], v[56:59]
	v_perm_b32 v27, v109, v108, s44
	v_mfma_f32_16x16x32_f16 v[60:63], a[204:207], v[176:179], v[60:63]
	v_perm_b32 v28, v111, v110, s44
	v_mfma_f32_16x16x32_f16 v[48:51], a[208:211], v[180:183], v[48:51]
	v_perm_b32 v96, v22, v21, s45
	v_mfma_f32_16x16x32_f16 v[52:55], a[212:215], v[180:183], v[52:55]
	v_perm_b32 v97, v24, v23, s45
	v_mfma_f32_16x16x32_f16 v[56:59], a[216:219], v[180:183], v[56:59]
	v_perm_b32 v98, v26, v25, s45
	v_mfma_f32_16x16x32_f16 v[60:63], a[220:223], v[180:183], v[60:63]
	v_perm_b32 v99, v28, v27, s45
	v_mfma_f32_16x16x32_f16 v[48:51], a[224:227], v[184:187], v[48:51]
	global_load_lds_dwordx4 v10, s[26:27] offset:1024
	global_store_dwordx4 v14, v[96:99], s[30:31]
	v_mfma_f32_16x16x32_f16 v[52:55], a[228:231], v[184:187], v[52:55]
	s_add_u32 s26, s26, 0x800
	s_addc_u32 s27, s27, 0
	global_store_dword v112, v20, s[30:31]
	v_mfma_f32_16x16x32_f16 v[56:59], a[232:235], v[184:187], v[56:59]
	v_mfma_f32_16x16x32_f16 v[60:63], a[236:239], v[184:187], v[60:63]
	s_add_u32 s30, s30, 0x8800
	s_addc_u32 s31, s31, 0
	v_mfma_f32_16x16x32_f16 v[48:51], a[240:243], v[188:191], v[48:51]
	v_mfma_f32_16x16x32_f16 v[52:55], a[244:247], v[188:191], v[52:55]
	v_mfma_f32_16x16x32_f16 v[56:59], a[248:251], v[188:191], v[56:59]
	v_mfma_f32_16x16x32_f16 v[60:63], a[252:255], v[188:191], v[60:63]
	s_sub_u32 s24, s24, 1
	s_cmp_le_u32 s24, 1
	s_cbranch_scc0 LgAq_loop
	s_nop 7
	s_nop 7
	v_max3_f32 v16, |v48|, 0, |v49|
	v_max3_f32 v16, v16, |v50|, |v51|
	v_max3_f32 v16, v16, |v52|, |v53|
	v_max3_f32 v16, v16, |v54|, |v55|
	v_max3_f32 v16, v16, |v56|, |v57|
	v_max3_f32 v16, v16, |v58|, |v59|
	v_max3_f32 v16, v16, |v60|, |v61|
	v_max3_f32 v16, v16, |v62|, |v63|
	v_mov_b32_e32 v17, v16
	v_mov_b32_e32 v18, v16
	s_nop 1
	v_permlane32_swap_b32_e32 v17, v18
	v_max_f32_e32 v16, v17, v18
	v_mov_b32_e32 v17, v16
	v_mov_b32_e32 v18, v16
	s_nop 1
	v_permlane16_swap_b32_e32 v17, v18
	v_max_f32_e32 v16, v17, v18
	v_rcp_f32_e32 v19, v16
	v_cmp_lt_f32_e32 vcc, 0, v16
	v_mul_f32_e32 v19, 0x42fe0000, v19
	v_mul_f32_e32 v20, 0x3c010204, v16
	v_cndmask_b32_e32 v19, 0, v19, vcc
	v_cndmask_b32_e32 v20, 1.0, v20, vcc
	v_fmaak_f32 v96, v19, v48, 0x4b400000
	v_fmaak_f32 v97, v19, v49, 0x4b400000
	v_fmaak_f32 v98, v19, v50, 0x4b400000
	v_fmaak_f32 v99, v19, v51, 0x4b400000
	v_fmaak_f32 v100, v19, v52, 0x4b400000
	v_fmaak_f32 v101, v19, v53, 0x4b400000
	v_fmaak_f32 v102, v19, v54, 0x4b400000
	v_fmaak_f32 v103, v19, v55, 0x4b400000
	v_fmaak_f32 v104, v19, v56, 0x4b400000
	v_fmaak_f32 v105, v19, v57, 0x4b400000
	v_fmaak_f32 v106, v19, v58, 0x4b400000
	v_fmaak_f32 v107, v19, v59, 0x4b400000
	v_fmaak_f32 v108, v19, v60, 0x4b400000
	v_fmaak_f32 v109, v19, v61, 0x4b400000
	v_fmaak_f32 v110, v19, v62, 0x4b400000
	v_fmaak_f32 v111, v19, v63, 0x4b400000
	v_perm_b32 v21, v97, v96, s44
	v_perm_b32 v22, v99, v98, s44
	v_perm_b32 v23, v101, v100, s44
	v_perm_b32 v24, v103, v102, s44
	v_perm_b32 v25, v105, v104, s44
	v_perm_b32 v26, v107, v106, s44
	v_perm_b32 v27, v109, v108, s44
	v_perm_b32 v28, v111, v110, s44
	v_perm_b32 v96, v22, v21, s45
	v_perm_b32 v97, v24, v23, s45
	v_perm_b32 v98, v26, v25, s45
	v_perm_b32 v99, v28, v27, s45
	global_store_dwordx4 v14, v[96:99], s[30:31]
	global_store_dword v112, v20, s[30:31]
	s_add_u32 s30, s30, 0x8800
	s_addc_u32 s31, s31, 0
	s_endpgm
